# baseline (speedup 1.0000x reference)
.LBB6_8:
	s_lshl_b32 s0, s19, 8
	s_add_i32 s21, s21, s0
	v_or_b32_e32 v0, s21, v141
	v_mov_b32_e32 v1, 0
	v_lshlrev_b64 v[132:133], 6, v[0:1]
	s_waitcnt lgkmcnt(0)
	v_lshl_add_u64 v[132:133], s[10:11], 0, v[132:133]
	s_barrier
	v_mov_b32_e32 v222, 0x2000
	v_mov_b32_e32 v223, 0
	v_mov_b32_e32 v224, s5
	v_lshl_add_u64 v[220:221], v[132:133], 0, v[222:223]
	global_load_dwordx4 v[148:151], v[132:133], off
	global_load_dwordx4 v[152:155], v[132:133], off offset:16
	global_load_dwordx4 v[156:159], v[132:133], off offset:32
	global_load_dwordx4 v[160:163], v[132:133], off offset:48
	global_load_dwordx4 v[164:167], v[132:133], off offset:1024
	global_load_dwordx4 v[168:171], v[132:133], off offset:1040
	global_load_dwordx4 v[172:175], v[132:133], off offset:1056
	global_load_dwordx4 v[176:179], v[132:133], off offset:1072
	global_load_dwordx4 v[180:183], v[132:133], off offset:2048
	global_load_dwordx4 v[184:187], v[132:133], off offset:2064
	global_load_dwordx4 v[188:191], v[132:133], off offset:2080
	global_load_dwordx4 v[192:195], v[132:133], off offset:2096
	global_load_dwordx4 v[196:199], v[132:133], off offset:3072
	global_load_dwordx4 v[200:203], v[132:133], off offset:3088
	global_load_dwordx4 v[204:207], v[132:133], off offset:3104
	global_load_dwordx4 v[208:211], v[132:133], off offset:3120
	s_waitcnt vmcnt(12)
	v_add_f32_e32 v148, v148, v149
	v_add_f32_e32 v150, v150, v151
	v_add_f32_e32 v148, v148, v150
	v_add_f32_e32 v152, v152, v153
	v_add_f32_e32 v154, v154, v155
	v_add_f32_e32 v152, v152, v154
	v_add_f32_e32 v156, v156, v157
	v_add_f32_e32 v158, v158, v159
	v_add_f32_e32 v156, v156, v158
	v_add_f32_e32 v160, v160, v161
	v_add_f32_e32 v162, v162, v163
	v_add_f32_e32 v160, v160, v162
	v_add_f32_e32 v148, v148, v152
	v_add_f32_e32 v156, v156, v160
	v_add_f32_e32 v148, v148, v156
	v_fma_f32 v148, s6, v148, v224
	v_rsq_f32_e32 v212, v148
	global_load_dwordx4 v[148:151], v[220:221], off
	global_load_dwordx4 v[152:155], v[220:221], off offset:16
	global_load_dwordx4 v[156:159], v[220:221], off offset:32
	global_load_dwordx4 v[160:163], v[220:221], off offset:48
	s_waitcnt vmcnt(12)
	v_add_f32_e32 v164, v164, v165
	v_add_f32_e32 v166, v166, v167
	v_add_f32_e32 v164, v164, v166
	v_add_f32_e32 v168, v168, v169
	v_add_f32_e32 v170, v170, v171
	v_add_f32_e32 v168, v168, v170
	v_add_f32_e32 v172, v172, v173
	v_add_f32_e32 v174, v174, v175
	v_add_f32_e32 v172, v172, v174
	v_add_f32_e32 v176, v176, v177
	v_add_f32_e32 v178, v178, v179
	v_add_f32_e32 v176, v176, v178
	v_add_f32_e32 v164, v164, v168
	v_add_f32_e32 v172, v172, v176
	v_add_f32_e32 v164, v164, v172
	v_fma_f32 v164, s6, v164, v224
	v_rsq_f32_e32 v213, v164
	global_load_dwordx4 v[164:167], v[220:221], off offset:1024
	global_load_dwordx4 v[168:171], v[220:221], off offset:1040
	global_load_dwordx4 v[172:175], v[220:221], off offset:1056
	global_load_dwordx4 v[176:179], v[220:221], off offset:1072
	s_waitcnt vmcnt(12)
	v_add_f32_e32 v180, v180, v181
	v_add_f32_e32 v182, v182, v183
	v_add_f32_e32 v180, v180, v182
	v_add_f32_e32 v184, v184, v185
	v_add_f32_e32 v186, v186, v187
	v_add_f32_e32 v184, v184, v186
	v_add_f32_e32 v188, v188, v189
	v_add_f32_e32 v190, v190, v191
	v_add_f32_e32 v188, v188, v190
	v_add_f32_e32 v192, v192, v193
	v_add_f32_e32 v194, v194, v195
	v_add_f32_e32 v192, v192, v194
	v_add_f32_e32 v180, v180, v184
	v_add_f32_e32 v188, v188, v192
	v_add_f32_e32 v180, v180, v188
	v_fma_f32 v180, s6, v180, v224
	v_rsq_f32_e32 v214, v180
	global_load_dwordx4 v[180:183], v[220:221], off offset:2048
	global_load_dwordx4 v[184:187], v[220:221], off offset:2064
	global_load_dwordx4 v[188:191], v[220:221], off offset:2080
	global_load_dwordx4 v[192:195], v[220:221], off offset:2096
	s_waitcnt vmcnt(12)
	v_add_f32_e32 v196, v196, v197
	v_add_f32_e32 v198, v198, v199
	v_add_f32_e32 v196, v196, v198
	v_add_f32_e32 v200, v200, v201
	v_add_f32_e32 v202, v202, v203
	v_add_f32_e32 v200, v200, v202
	v_add_f32_e32 v204, v204, v205
	v_add_f32_e32 v206, v206, v207
	v_add_f32_e32 v204, v204, v206
	v_add_f32_e32 v208, v208, v209
	v_add_f32_e32 v210, v210, v211
	v_add_f32_e32 v208, v208, v210
	v_add_f32_e32 v196, v196, v200
	v_add_f32_e32 v204, v204, v208
	v_add_f32_e32 v196, v196, v204
	v_fma_f32 v196, s6, v196, v224
	v_rsq_f32_e32 v215, v196
	global_load_dwordx4 v[196:199], v[220:221], off offset:3072
	global_load_dwordx4 v[200:203], v[220:221], off offset:3088
	global_load_dwordx4 v[204:207], v[220:221], off offset:3104
	global_load_dwordx4 v[208:211], v[220:221], off offset:3120
	s_waitcnt vmcnt(12)
	v_add_f32_e32 v148, v148, v149
	v_add_f32_e32 v150, v150, v151
	v_add_f32_e32 v148, v148, v150
	v_add_f32_e32 v152, v152, v153
	v_add_f32_e32 v154, v154, v155
	v_add_f32_e32 v152, v152, v154
	v_add_f32_e32 v156, v156, v157
	v_add_f32_e32 v158, v158, v159
	v_add_f32_e32 v156, v156, v158
	v_add_f32_e32 v160, v160, v161
	v_add_f32_e32 v162, v162, v163
	v_add_f32_e32 v160, v160, v162
	v_add_f32_e32 v148, v148, v152
	v_add_f32_e32 v156, v156, v160
	v_add_f32_e32 v148, v148, v156
	v_fma_f32 v148, s6, v148, v224
	v_rsq_f32_e32 v216, v148
	s_waitcnt vmcnt(8)
	v_add_f32_e32 v164, v164, v165
	v_add_f32_e32 v166, v166, v167
	v_add_f32_e32 v164, v164, v166
	v_add_f32_e32 v168, v168, v169
	v_add_f32_e32 v170, v170, v171
	v_add_f32_e32 v168, v168, v170
	v_add_f32_e32 v172, v172, v173
	v_add_f32_e32 v174, v174, v175
	v_add_f32_e32 v172, v172, v174
	v_add_f32_e32 v176, v176, v177
	v_add_f32_e32 v178, v178, v179
	v_add_f32_e32 v176, v176, v178
	v_add_f32_e32 v164, v164, v168
	v_add_f32_e32 v172, v172, v176
	v_add_f32_e32 v164, v164, v172
	v_fma_f32 v164, s6, v164, v224
	v_rsq_f32_e32 v217, v164
	s_waitcnt vmcnt(4)
	v_add_f32_e32 v180, v180, v181
	v_add_f32_e32 v182, v182, v183
	v_add_f32_e32 v180, v180, v182
	v_add_f32_e32 v184, v184, v185
	v_add_f32_e32 v186, v186, v187
	v_add_f32_e32 v184, v184, v186
	v_add_f32_e32 v188, v188, v189
	v_add_f32_e32 v190, v190, v191
	v_add_f32_e32 v188, v188, v190
	v_add_f32_e32 v192, v192, v193
	v_add_f32_e32 v194, v194, v195
	v_add_f32_e32 v192, v192, v194
	v_add_f32_e32 v180, v180, v184
	v_add_f32_e32 v188, v188, v192
	v_add_f32_e32 v180, v180, v188
	v_fma_f32 v180, s6, v180, v224
	v_rsq_f32_e32 v218, v180
	s_waitcnt vmcnt(0)
	v_add_f32_e32 v196, v196, v197
	v_add_f32_e32 v198, v198, v199
	v_add_f32_e32 v196, v196, v198
	v_add_f32_e32 v200, v200, v201
	v_add_f32_e32 v202, v202, v203
	v_add_f32_e32 v200, v200, v202
	v_add_f32_e32 v204, v204, v205
	v_add_f32_e32 v206, v206, v207
	v_add_f32_e32 v204, v204, v206
	v_add_f32_e32 v208, v208, v209
	v_add_f32_e32 v210, v210, v211
	v_add_f32_e32 v208, v208, v210
	v_add_f32_e32 v196, v196, v200
	v_add_f32_e32 v204, v204, v208
	v_add_f32_e32 v196, v196, v204
	v_fma_f32 v196, s6, v196, v224
	v_rsq_f32_e32 v219, v196
	s_lshl_b32 s1, s18, 8
	s_or_b32 s1, s7, s1
	v_or_b32_e32 v130, s1, v140
	v_mov_b32_e32 v132, s5
	v_mov_b32_e32 v129, v131
	s_mov_b32 s0, 0xc0135761
	v_mad_i64_i32 v[138:139], s[2:3], v0, s4, 0
	v_ashrrev_i32_e32 v131, 31, v130
	v_lshlrev_b64 v[130:131], 1, v[130:131]
	s_nop 0
	v_lshl_add_u64 v[136:137], v[138:139], 1, s[8:9]
	v_mov_b32_e32 v134, v212
	v_lshl_add_u64 v[136:137], v[136:137], 0, v[130:131]
	v_pk_mul_f32 v[126:127], v[126:127], v[134:135] op_sel_hi:[1,0]
	v_pk_mul_f32 v[128:129], v[128:129], v[134:135] op_sel_hi:[1,0]
	v_pk_mul_f32 v[122:123], v[122:123], v[134:135] op_sel_hi:[1,0]
	v_pk_mul_f32 v[124:125], v[124:125], v[134:135] op_sel_hi:[1,0]
	v_pk_mul_f32 v[118:119], v[118:119], v[134:135] op_sel_hi:[1,0]
	v_mul_f32_e32 v133, 0x3dd2d3e8, v126
	v_mul_f32_e32 v135, 0x3dd2d3e8, v127
	v_mul_f32_e32 v138, 0x3dd2d3e8, v128
	v_mul_f32_e32 v139, 0x3dd2d3e8, v129
	v_mul_f32_e32 v140, 0x3dd2d3e8, v122
	v_mul_f32_e32 v141, 0x3dd2d3e8, v123
	v_fma_f32 v133, -v126, v133, s0
	v_fma_f32 v135, -v127, v135, s0
	v_mul_f32_e32 v142, 0x3dd2d3e8, v124
	v_mul_f32_e32 v143, 0x3dd2d3e8, v125
	v_fma_f32 v138, -v128, v138, s0
	v_fma_f32 v139, -v129, v139, s0
	v_fma_f32 v140, -v122, v140, s0
	v_fma_f32 v141, -v123, v141, s0
	v_mul_f32_e32 v133, v126, v133
	v_mul_f32_e32 v135, v127, v135
	v_fma_f32 v142, -v124, v142, s0
	v_fma_f32 v143, -v125, v143, s0
	v_mul_f32_e32 v138, v128, v138
	v_mul_f32_e32 v139, v129, v139
	v_mul_f32_e32 v140, v122, v140
	v_mul_f32_e32 v141, v123, v141
	v_exp_f32_e32 v133, v133
	v_exp_f32_e32 v135, v135
	v_mul_f32_e32 v142, v124, v142
	v_mul_f32_e32 v143, v125, v143
	v_exp_f32_e32 v138, v138
	v_exp_f32_e32 v139, v139
	v_exp_f32_e32 v140, v140
	v_exp_f32_e32 v141, v141
	v_mul_f32_e32 v144, 0x3dd2d3e8, v118
	v_exp_f32_e32 v142, v142
	v_exp_f32_e32 v143, v143
	v_fma_f32 v144, -v118, v144, s0
	v_mul_f32_e32 v144, v118, v144
	v_add_f32_e32 v133, 1.0, v133
	v_add_f32_e32 v135, 1.0, v135
	v_exp_f32_e32 v146, v144
	v_add_f32_e32 v144, 1.0, v138
	v_add_f32_e32 v145, 1.0, v139
	v_add_f32_e32 v147, 1.0, v140
	v_add_f32_e32 v148, 1.0, v141
	v_rcp_f32_e32 v138, v133
	v_rcp_f32_e32 v139, v135
	v_add_f32_e32 v149, 1.0, v142
	v_add_f32_e32 v150, 1.0, v143
	v_rcp_f32_e32 v142, v147
	v_rcp_f32_e32 v143, v148
	v_pk_mul_f32 v[126:127], v[126:127], v[138:139]
	v_rcp_f32_e32 v140, v144
	v_rcp_f32_e32 v141, v145
	v_pk_mul_f32 v[138:139], v[122:123], v[142:143]
	v_cvt_pk_bf16_f32 v122, v126, v127
	v_mul_f32_e32 v126, 0x3dd2d3e8, v119
	v_rcp_f32_e32 v144, v149
	v_rcp_f32_e32 v145, v150
	v_fma_f32 v126, -v119, v126, s0
	v_mul_f32_e32 v126, v119, v126
	v_exp_f32_e32 v126, v126
	v_pk_mul_f32 v[128:129], v[128:129], v[140:141]
	v_pk_mul_f32 v[140:141], v[124:125], v[144:145]
	v_cvt_pk_bf16_f32 v123, v128, v129
	v_cvt_pk_bf16_f32 v124, v138, v139
	v_cvt_pk_bf16_f32 v125, v140, v141
	v_pk_mul_f32 v[120:121], v[120:121], v[134:135] op_sel_hi:[1,0]
	v_pk_mul_f32 v[114:115], v[114:115], v[134:135] op_sel_hi:[1,0]
	v_pk_mul_f32 v[116:117], v[116:117], v[134:135] op_sel_hi:[1,0]
	global_store_dwordx4 v[136:137], v[122:125], off
	v_mul_f32_e32 v127, 0x3dd2d3e8, v115
	v_mul_f32_e32 v128, 0x3dd2d3e8, v116
	v_add_f32_e32 v123, 1.0, v126
	v_mul_f32_e32 v124, 0x3dd2d3e8, v120
	v_mul_f32_e32 v125, 0x3dd2d3e8, v121
	v_mul_f32_e32 v126, 0x3dd2d3e8, v114
	v_mul_f32_e32 v129, 0x3dd2d3e8, v117
	v_fma_f32 v124, -v120, v124, s0
	v_fma_f32 v125, -v121, v125, s0
	v_fma_f32 v126, -v114, v126, s0
	v_fma_f32 v127, -v115, v127, s0
	v_fma_f32 v128, -v116, v128, s0
	v_fma_f32 v129, -v117, v129, s0
	v_mul_f32_e32 v124, v120, v124
	v_mul_f32_e32 v125, v121, v125
	v_mul_f32_e32 v126, v114, v126
	v_mul_f32_e32 v127, v115, v127
	v_mul_f32_e32 v128, v116, v128
	v_mul_f32_e32 v129, v117, v129
	v_exp_f32_e32 v124, v124
	v_exp_f32_e32 v125, v125
	v_exp_f32_e32 v126, v126
	v_exp_f32_e32 v127, v127
	v_exp_f32_e32 v128, v128
	v_exp_f32_e32 v129, v129
	v_add_f32_e32 v122, 1.0, v146
	v_add_f32_e32 v124, 1.0, v124
	v_add_f32_e32 v125, 1.0, v125
	v_add_f32_e32 v126, 1.0, v126
	v_add_f32_e32 v127, 1.0, v127
	v_add_f32_e32 v128, 1.0, v128
	v_add_f32_e32 v129, 1.0, v129
	v_rcp_f32_e32 v122, v122
	v_rcp_f32_e32 v123, v123
	v_rcp_f32_e32 v124, v124
	v_rcp_f32_e32 v125, v125
	v_rcp_f32_e32 v126, v126
	v_rcp_f32_e32 v127, v127
	v_rcp_f32_e32 v128, v128
	v_rcp_f32_e32 v129, v129
	v_pk_mul_f32 v[118:119], v[118:119], v[122:123]
	v_pk_mul_f32 v[120:121], v[120:121], v[124:125]
	v_pk_mul_f32 v[122:123], v[114:115], v[126:127]
	v_pk_mul_f32 v[124:125], v[116:117], v[128:129]
	v_cvt_pk_bf16_f32 v114, v118, v119
	v_cvt_pk_bf16_f32 v115, v120, v121
	v_cvt_pk_bf16_f32 v116, v122, v123
	v_cvt_pk_bf16_f32 v117, v124, v125
	v_or_b32_e32 v134, 16, v0
	v_mov_b32_e32 v135, v1
	global_store_dwordx4 v[136:137], v[114:117], off offset:256
	s_nop 1
	v_lshlrev_b64 v[114:115], 6, v[134:135]
	v_lshl_add_u64 v[126:127], s[10:11], 0, v[114:115]
	s_nop 0
	s_nop 0
	v_mad_i64_i32 v[116:117], s[2:3], v134, s4, 0
	v_mov_b32_e32 v114, v213
	v_lshl_add_u64 v[116:117], v[116:117], 1, s[8:9]
	v_lshl_add_u64 v[116:117], v[116:117], 0, v[130:131]
	v_pk_mul_f32 v[110:111], v[110:111], v[114:115] op_sel_hi:[1,0]
	s_nop 0
	v_mul_f32_e32 v115, 0x3dd2d3e8, v110
	v_mul_f32_e32 v118, 0x3dd2d3e8, v111
	v_fma_f32 v115, -v110, v115, s0
	v_mul_f32_e32 v115, v110, v115
	v_fma_f32 v118, -v111, v118, s0
	v_exp_f32_e32 v115, v115
	v_mul_f32_e32 v118, v111, v118
	v_exp_f32_e32 v119, v118
	v_add_f32_e32 v115, 1.0, v115
	v_rcp_f32_e32 v118, v115
	v_add_f32_e32 v115, 1.0, v119
	v_pk_mul_f32 v[112:113], v[112:113], v[114:115] op_sel_hi:[1,0]
	s_nop 0
	v_mul_f32_e32 v119, 0x3dd2d3e8, v112
	v_fma_f32 v119, -v112, v119, s0
	v_mul_f32_e32 v119, v112, v119
	v_exp_f32_e32 v120, v119
	v_mul_f32_e32 v119, 0x3dd2d3e8, v113
	v_fma_f32 v119, -v113, v119, s0
	v_mul_f32_e32 v119, v113, v119
	v_exp_f32_e32 v121, v119
	v_rcp_f32_e32 v119, v115
	v_add_f32_e32 v115, 1.0, v120
	v_rcp_f32_e32 v120, v115
	v_add_f32_e32 v115, 1.0, v121
	v_pk_mul_f32 v[106:107], v[106:107], v[114:115] op_sel_hi:[1,0]
	v_pk_mul_f32 v[110:111], v[110:111], v[118:119]
	v_mul_f32_e32 v121, 0x3dd2d3e8, v106
	v_fma_f32 v121, -v106, v121, s0
	v_mul_f32_e32 v121, v106, v121
	v_exp_f32_e32 v122, v121
	v_mul_f32_e32 v121, 0x3dd2d3e8, v107
	v_fma_f32 v121, -v107, v121, s0
	v_mul_f32_e32 v121, v107, v121
	v_exp_f32_e32 v123, v121
	v_rcp_f32_e32 v121, v115
	v_add_f32_e32 v115, 1.0, v122
	v_rcp_f32_e32 v122, v115
	v_add_f32_e32 v115, 1.0, v123
	v_pk_mul_f32 v[108:109], v[108:109], v[114:115] op_sel_hi:[1,0]
	v_pk_mul_f32 v[112:113], v[112:113], v[120:121]
	v_mul_f32_e32 v123, 0x3dd2d3e8, v108
	v_fma_f32 v123, -v108, v123, s0
	v_mul_f32_e32 v123, v108, v123
	v_exp_f32_e32 v124, v123
	v_mul_f32_e32 v123, 0x3dd2d3e8, v109
	v_fma_f32 v123, -v109, v123, s0
	v_mul_f32_e32 v123, v109, v123
	v_exp_f32_e32 v125, v123
	v_rcp_f32_e32 v123, v115
	v_add_f32_e32 v115, 1.0, v124
	v_rcp_f32_e32 v124, v115
	v_add_f32_e32 v115, 1.0, v125
	v_pk_mul_f32 v[102:103], v[102:103], v[114:115] op_sel_hi:[1,0]
	v_pk_mul_f32 v[118:119], v[106:107], v[122:123]
	v_cvt_pk_bf16_f32 v106, v110, v111
	v_mul_f32_e32 v110, 0x3dd2d3e8, v102
	v_mul_f32_e32 v111, 0x3dd2d3e8, v103
	v_rcp_f32_e32 v125, v115
	v_fma_f32 v110, -v102, v110, s0
	v_fma_f32 v111, -v103, v111, s0
	v_mul_f32_e32 v110, v102, v110
	v_mul_f32_e32 v111, v103, v111
	v_exp_f32_e32 v110, v110
	v_exp_f32_e32 v111, v111
	v_pk_mul_f32 v[120:121], v[108:109], v[124:125]
	v_cvt_pk_bf16_f32 v107, v112, v113
	v_cvt_pk_bf16_f32 v108, v118, v119
	v_cvt_pk_bf16_f32 v109, v120, v121
	v_pk_mul_f32 v[104:105], v[104:105], v[114:115] op_sel_hi:[1,0]
	v_pk_mul_f32 v[98:99], v[98:99], v[114:115] op_sel_hi:[1,0]
	v_pk_mul_f32 v[100:101], v[100:101], v[114:115] op_sel_hi:[1,0]
	global_store_dwordx4 v[116:117], v[106:109], off
	v_mul_f32_e32 v112, 0x3dd2d3e8, v100
	v_mul_f32_e32 v113, 0x3dd2d3e8, v101
	v_add_f32_e32 v106, 1.0, v110
	v_add_f32_e32 v107, 1.0, v111
	v_mul_f32_e32 v108, 0x3dd2d3e8, v104
	v_mul_f32_e32 v109, 0x3dd2d3e8, v105
	v_mul_f32_e32 v110, 0x3dd2d3e8, v98
	v_mul_f32_e32 v111, 0x3dd2d3e8, v99
	v_fma_f32 v108, -v104, v108, s0
	v_fma_f32 v109, -v105, v109, s0
	v_fma_f32 v110, -v98, v110, s0
	v_fma_f32 v111, -v99, v111, s0
	v_fma_f32 v112, -v100, v112, s0
	v_fma_f32 v113, -v101, v113, s0
	v_mul_f32_e32 v108, v104, v108
	v_mul_f32_e32 v109, v105, v109
	v_mul_f32_e32 v110, v98, v110
	v_mul_f32_e32 v111, v99, v111
	v_mul_f32_e32 v112, v100, v112
	v_mul_f32_e32 v113, v101, v113
	v_exp_f32_e32 v108, v108
	v_exp_f32_e32 v109, v109
	v_exp_f32_e32 v110, v110
	v_exp_f32_e32 v111, v111
	v_exp_f32_e32 v112, v112
	v_exp_f32_e32 v113, v113
	v_add_f32_e32 v108, 1.0, v108
	v_add_f32_e32 v109, 1.0, v109
	v_add_f32_e32 v110, 1.0, v110
	v_add_f32_e32 v111, 1.0, v111
	v_add_f32_e32 v112, 1.0, v112
	v_add_f32_e32 v113, 1.0, v113
	v_rcp_f32_e32 v106, v106
	v_rcp_f32_e32 v107, v107
	v_rcp_f32_e32 v108, v108
	v_rcp_f32_e32 v109, v109
	v_rcp_f32_e32 v110, v110
	v_rcp_f32_e32 v111, v111
	v_rcp_f32_e32 v112, v112
	v_rcp_f32_e32 v113, v113
	v_pk_mul_f32 v[102:103], v[102:103], v[106:107]
	v_pk_mul_f32 v[104:105], v[104:105], v[108:109]
	v_pk_mul_f32 v[106:107], v[98:99], v[110:111]
	v_pk_mul_f32 v[108:109], v[100:101], v[112:113]
	v_cvt_pk_bf16_f32 v98, v102, v103
	v_cvt_pk_bf16_f32 v99, v104, v105
	v_cvt_pk_bf16_f32 v100, v106, v107
	v_cvt_pk_bf16_f32 v101, v108, v109
	v_or_b32_e32 v114, 32, v0
	v_mov_b32_e32 v115, v1
	global_store_dwordx4 v[116:117], v[98:101], off offset:256
	s_nop 1
	v_lshlrev_b64 v[98:99], 6, v[114:115]
	v_lshl_add_u64 v[116:117], s[10:11], 0, v[98:99]
	s_nop 0
	s_nop 0
	v_mad_i64_i32 v[100:101], s[2:3], v114, s4, 0
	v_mov_b32_e32 v98, v214
	v_lshl_add_u64 v[100:101], v[100:101], 1, s[8:9]
	v_lshl_add_u64 v[100:101], v[100:101], 0, v[130:131]
	v_pk_mul_f32 v[94:95], v[94:95], v[98:99] op_sel_hi:[1,0]
	s_nop 0
	v_mul_f32_e32 v99, 0x3dd2d3e8, v94
	v_fma_f32 v99, -v94, v99, s0
	v_mul_f32_e32 v102, 0x3dd2d3e8, v95
	v_mul_f32_e32 v99, v94, v99
	v_fma_f32 v102, -v95, v102, s0
	v_exp_f32_e32 v99, v99
	v_mul_f32_e32 v102, v95, v102
	v_exp_f32_e32 v103, v102
	v_add_f32_e32 v99, 1.0, v99
	v_rcp_f32_e32 v102, v99
	v_add_f32_e32 v99, 1.0, v103
	v_pk_mul_f32 v[96:97], v[96:97], v[98:99] op_sel_hi:[1,0]
	s_nop 0
	v_mul_f32_e32 v103, 0x3dd2d3e8, v96
	v_fma_f32 v103, -v96, v103, s0
	v_mul_f32_e32 v103, v96, v103
	v_exp_f32_e32 v104, v103
	v_mul_f32_e32 v103, 0x3dd2d3e8, v97
	v_fma_f32 v103, -v97, v103, s0
	v_mul_f32_e32 v103, v97, v103
	v_exp_f32_e32 v105, v103
	v_rcp_f32_e32 v103, v99
	v_add_f32_e32 v99, 1.0, v104
	v_rcp_f32_e32 v104, v99
	v_add_f32_e32 v99, 1.0, v105
	v_pk_mul_f32 v[90:91], v[90:91], v[98:99] op_sel_hi:[1,0]
	v_pk_mul_f32 v[94:95], v[94:95], v[102:103]
	v_mul_f32_e32 v105, 0x3dd2d3e8, v90
	v_fma_f32 v105, -v90, v105, s0
	v_mul_f32_e32 v105, v90, v105
	v_exp_f32_e32 v106, v105
	v_mul_f32_e32 v105, 0x3dd2d3e8, v91
	v_fma_f32 v105, -v91, v105, s0
	v_mul_f32_e32 v105, v91, v105
	v_exp_f32_e32 v107, v105
	v_rcp_f32_e32 v105, v99
	v_add_f32_e32 v99, 1.0, v106
	v_rcp_f32_e32 v106, v99
	v_add_f32_e32 v99, 1.0, v107
	v_pk_mul_f32 v[92:93], v[92:93], v[98:99] op_sel_hi:[1,0]
	v_pk_mul_f32 v[96:97], v[96:97], v[104:105]
	v_mul_f32_e32 v107, 0x3dd2d3e8, v92
	v_fma_f32 v107, -v92, v107, s0
	v_mul_f32_e32 v107, v92, v107
	v_exp_f32_e32 v108, v107
	v_mul_f32_e32 v107, 0x3dd2d3e8, v93
	v_fma_f32 v107, -v93, v107, s0
	v_mul_f32_e32 v107, v93, v107
	v_exp_f32_e32 v109, v107
	v_rcp_f32_e32 v107, v99
	v_add_f32_e32 v99, 1.0, v108
	v_rcp_f32_e32 v108, v99
	v_add_f32_e32 v99, 1.0, v109
	v_pk_mul_f32 v[86:87], v[86:87], v[98:99] op_sel_hi:[1,0]
	v_pk_mul_f32 v[102:103], v[90:91], v[106:107]
	v_cvt_pk_bf16_f32 v90, v94, v95
	v_mul_f32_e32 v94, 0x3dd2d3e8, v86
	v_mul_f32_e32 v95, 0x3dd2d3e8, v87
	v_rcp_f32_e32 v109, v99
	v_fma_f32 v94, -v86, v94, s0
	v_fma_f32 v95, -v87, v95, s0
	v_mul_f32_e32 v94, v86, v94
	v_mul_f32_e32 v95, v87, v95
	v_exp_f32_e32 v94, v94
	v_exp_f32_e32 v95, v95
	v_pk_mul_f32 v[104:105], v[92:93], v[108:109]
	v_cvt_pk_bf16_f32 v91, v96, v97
	v_cvt_pk_bf16_f32 v92, v102, v103
	v_cvt_pk_bf16_f32 v93, v104, v105
	v_pk_mul_f32 v[88:89], v[88:89], v[98:99] op_sel_hi:[1,0]
	v_pk_mul_f32 v[82:83], v[82:83], v[98:99] op_sel_hi:[1,0]
	v_pk_mul_f32 v[84:85], v[84:85], v[98:99] op_sel_hi:[1,0]
	global_store_dwordx4 v[100:101], v[90:93], off
	v_mul_f32_e32 v96, 0x3dd2d3e8, v84
	v_mul_f32_e32 v97, 0x3dd2d3e8, v85
	v_add_f32_e32 v90, 1.0, v94
	v_add_f32_e32 v91, 1.0, v95
	v_mul_f32_e32 v92, 0x3dd2d3e8, v88
	v_mul_f32_e32 v93, 0x3dd2d3e8, v89
	v_mul_f32_e32 v94, 0x3dd2d3e8, v82
	v_mul_f32_e32 v95, 0x3dd2d3e8, v83
	v_fma_f32 v92, -v88, v92, s0
	v_fma_f32 v93, -v89, v93, s0
	v_fma_f32 v94, -v82, v94, s0
	v_fma_f32 v95, -v83, v95, s0
	v_fma_f32 v96, -v84, v96, s0
	v_fma_f32 v97, -v85, v97, s0
	v_mul_f32_e32 v92, v88, v92
	v_mul_f32_e32 v93, v89, v93
	v_mul_f32_e32 v94, v82, v94
	v_mul_f32_e32 v95, v83, v95
	v_mul_f32_e32 v96, v84, v96
	v_mul_f32_e32 v97, v85, v97
	v_exp_f32_e32 v92, v92
	v_exp_f32_e32 v93, v93
	v_exp_f32_e32 v94, v94
	v_exp_f32_e32 v95, v95
	v_exp_f32_e32 v96, v96
	v_exp_f32_e32 v97, v97
	v_add_f32_e32 v92, 1.0, v92
	v_add_f32_e32 v93, 1.0, v93
	v_add_f32_e32 v94, 1.0, v94
	v_add_f32_e32 v95, 1.0, v95
	v_add_f32_e32 v96, 1.0, v96
	v_add_f32_e32 v97, 1.0, v97
	v_rcp_f32_e32 v90, v90
	v_rcp_f32_e32 v91, v91
	v_rcp_f32_e32 v92, v92
	v_rcp_f32_e32 v93, v93
	v_rcp_f32_e32 v94, v94
	v_rcp_f32_e32 v95, v95
	v_rcp_f32_e32 v96, v96
	v_rcp_f32_e32 v97, v97
	v_pk_mul_f32 v[86:87], v[86:87], v[90:91]
	v_pk_mul_f32 v[88:89], v[88:89], v[92:93]
	v_pk_mul_f32 v[90:91], v[82:83], v[94:95]
	v_pk_mul_f32 v[92:93], v[84:85], v[96:97]
	v_cvt_pk_bf16_f32 v82, v86, v87
	v_cvt_pk_bf16_f32 v83, v88, v89
	v_cvt_pk_bf16_f32 v84, v90, v91
	v_cvt_pk_bf16_f32 v85, v92, v93
	v_or_b32_e32 v98, 48, v0
	v_mov_b32_e32 v99, v1
	global_store_dwordx4 v[100:101], v[82:85], off offset:256
	s_nop 1
	v_lshlrev_b64 v[82:83], 6, v[98:99]
	v_lshl_add_u64 v[100:101], s[10:11], 0, v[82:83]
	s_nop 0
	s_nop 0
	v_mad_i64_i32 v[84:85], s[2:3], v98, s4, 0
	v_mov_b32_e32 v82, v215
	v_lshl_add_u64 v[84:85], v[84:85], 1, s[8:9]
	v_lshl_add_u64 v[84:85], v[84:85], 0, v[130:131]
	v_pk_mul_f32 v[78:79], v[78:79], v[82:83] op_sel_hi:[1,0]
	s_nop 0
	v_mul_f32_e32 v83, 0x3dd2d3e8, v78
	v_fma_f32 v83, -v78, v83, s0
	v_mul_f32_e32 v86, 0x3dd2d3e8, v79
	v_mul_f32_e32 v83, v78, v83
	v_fma_f32 v86, -v79, v86, s0
	v_exp_f32_e32 v83, v83
	v_mul_f32_e32 v86, v79, v86
	v_exp_f32_e32 v87, v86
	v_add_f32_e32 v83, 1.0, v83
	v_rcp_f32_e32 v86, v83
	v_add_f32_e32 v83, 1.0, v87
	v_pk_mul_f32 v[80:81], v[80:81], v[82:83] op_sel_hi:[1,0]
	s_nop 0
	v_mul_f32_e32 v87, 0x3dd2d3e8, v80
	v_fma_f32 v87, -v80, v87, s0
	v_mul_f32_e32 v87, v80, v87
	v_exp_f32_e32 v88, v87
	v_mul_f32_e32 v87, 0x3dd2d3e8, v81
	v_fma_f32 v87, -v81, v87, s0
	v_mul_f32_e32 v87, v81, v87
	v_exp_f32_e32 v89, v87
	v_rcp_f32_e32 v87, v83
	v_add_f32_e32 v83, 1.0, v88
	v_rcp_f32_e32 v88, v83
	v_add_f32_e32 v83, 1.0, v89
	v_pk_mul_f32 v[74:75], v[74:75], v[82:83] op_sel_hi:[1,0]
	v_pk_mul_f32 v[78:79], v[78:79], v[86:87]
	v_mul_f32_e32 v89, 0x3dd2d3e8, v74
	v_fma_f32 v89, -v74, v89, s0
	v_mul_f32_e32 v89, v74, v89
	v_exp_f32_e32 v90, v89
	v_mul_f32_e32 v89, 0x3dd2d3e8, v75
	v_fma_f32 v89, -v75, v89, s0
	v_mul_f32_e32 v89, v75, v89
	v_exp_f32_e32 v91, v89
	v_rcp_f32_e32 v89, v83
	v_add_f32_e32 v83, 1.0, v90
	v_rcp_f32_e32 v90, v83
	v_add_f32_e32 v83, 1.0, v91
	v_pk_mul_f32 v[76:77], v[76:77], v[82:83] op_sel_hi:[1,0]
	v_pk_mul_f32 v[80:81], v[80:81], v[88:89]
	v_mul_f32_e32 v91, 0x3dd2d3e8, v76
	v_fma_f32 v91, -v76, v91, s0
	v_mul_f32_e32 v91, v76, v91
	v_exp_f32_e32 v92, v91
	v_mul_f32_e32 v91, 0x3dd2d3e8, v77
	v_fma_f32 v91, -v77, v91, s0
	v_mul_f32_e32 v91, v77, v91
	v_exp_f32_e32 v93, v91
	v_rcp_f32_e32 v91, v83
	v_add_f32_e32 v83, 1.0, v92
	v_rcp_f32_e32 v92, v83
	v_add_f32_e32 v83, 1.0, v93
	v_pk_mul_f32 v[70:71], v[70:71], v[82:83] op_sel_hi:[1,0]
	v_pk_mul_f32 v[86:87], v[74:75], v[90:91]
	v_cvt_pk_bf16_f32 v74, v78, v79
	v_mul_f32_e32 v78, 0x3dd2d3e8, v70
	v_mul_f32_e32 v79, 0x3dd2d3e8, v71
	v_rcp_f32_e32 v93, v83
	v_fma_f32 v78, -v70, v78, s0
	v_fma_f32 v79, -v71, v79, s0
	v_mul_f32_e32 v78, v70, v78
	v_mul_f32_e32 v79, v71, v79
	v_exp_f32_e32 v78, v78
	v_exp_f32_e32 v79, v79
	v_pk_mul_f32 v[88:89], v[76:77], v[92:93]
	v_cvt_pk_bf16_f32 v75, v80, v81
	v_cvt_pk_bf16_f32 v76, v86, v87
	v_cvt_pk_bf16_f32 v77, v88, v89
	v_pk_mul_f32 v[72:73], v[72:73], v[82:83] op_sel_hi:[1,0]
	v_pk_mul_f32 v[66:67], v[66:67], v[82:83] op_sel_hi:[1,0]
	v_pk_mul_f32 v[68:69], v[68:69], v[82:83] op_sel_hi:[1,0]
	global_store_dwordx4 v[84:85], v[74:77], off
	v_mul_f32_e32 v80, 0x3dd2d3e8, v68
	v_mul_f32_e32 v81, 0x3dd2d3e8, v69
	v_add_f32_e32 v74, 1.0, v78
	v_add_f32_e32 v75, 1.0, v79
	v_mul_f32_e32 v76, 0x3dd2d3e8, v72
	v_mul_f32_e32 v77, 0x3dd2d3e8, v73
	v_mul_f32_e32 v78, 0x3dd2d3e8, v66
	v_mul_f32_e32 v79, 0x3dd2d3e8, v67
	v_fma_f32 v76, -v72, v76, s0
	v_fma_f32 v77, -v73, v77, s0
	v_fma_f32 v78, -v66, v78, s0
	v_fma_f32 v79, -v67, v79, s0
	v_fma_f32 v80, -v68, v80, s0
	v_fma_f32 v81, -v69, v81, s0
	v_mul_f32_e32 v76, v72, v76
	v_mul_f32_e32 v77, v73, v77
	v_mul_f32_e32 v78, v66, v78
	v_mul_f32_e32 v79, v67, v79
	v_mul_f32_e32 v80, v68, v80
	v_mul_f32_e32 v81, v69, v81
	v_exp_f32_e32 v76, v76
	v_exp_f32_e32 v77, v77
	v_exp_f32_e32 v78, v78
	v_exp_f32_e32 v79, v79
	v_exp_f32_e32 v80, v80
	v_exp_f32_e32 v81, v81
	v_add_f32_e32 v76, 1.0, v76
	v_add_f32_e32 v77, 1.0, v77
	v_add_f32_e32 v78, 1.0, v78
	v_add_f32_e32 v79, 1.0, v79
	v_add_f32_e32 v80, 1.0, v80
	v_add_f32_e32 v81, 1.0, v81
	v_rcp_f32_e32 v74, v74
	v_rcp_f32_e32 v75, v75
	v_rcp_f32_e32 v76, v76
	v_rcp_f32_e32 v77, v77
	v_rcp_f32_e32 v78, v78
	v_rcp_f32_e32 v79, v79
	v_rcp_f32_e32 v80, v80
	v_rcp_f32_e32 v81, v81
	v_pk_mul_f32 v[70:71], v[70:71], v[74:75]
	v_pk_mul_f32 v[72:73], v[72:73], v[76:77]
	v_pk_mul_f32 v[74:75], v[66:67], v[78:79]
	v_pk_mul_f32 v[76:77], v[68:69], v[80:81]
	v_cvt_pk_bf16_f32 v66, v70, v71
	v_cvt_pk_bf16_f32 v67, v72, v73
	v_cvt_pk_bf16_f32 v68, v74, v75
	v_cvt_pk_bf16_f32 v69, v76, v77
	v_add_u32_e32 v82, 0x80, v0
	v_mov_b32_e32 v83, v1
	global_store_dwordx4 v[84:85], v[66:69], off offset:256
	s_nop 1
	v_lshlrev_b64 v[66:67], 6, v[82:83]
	v_lshl_add_u64 v[84:85], s[10:11], 0, v[66:67]
	s_nop 0
	s_nop 0
	v_mad_i64_i32 v[68:69], s[2:3], v82, s4, 0
	v_mov_b32_e32 v66, v216
	v_lshl_add_u64 v[68:69], v[68:69], 1, s[8:9]
	v_lshl_add_u64 v[68:69], v[68:69], 0, v[130:131]
	v_pk_mul_f32 v[62:63], v[62:63], v[66:67] op_sel_hi:[1,0]
	s_nop 0
	v_mul_f32_e32 v67, 0x3dd2d3e8, v62
	v_fma_f32 v67, -v62, v67, s0
	v_mul_f32_e32 v70, 0x3dd2d3e8, v63
	v_mul_f32_e32 v67, v62, v67
	v_fma_f32 v70, -v63, v70, s0
	v_exp_f32_e32 v67, v67
	v_mul_f32_e32 v70, v63, v70
	v_exp_f32_e32 v71, v70
	v_add_f32_e32 v67, 1.0, v67
	v_rcp_f32_e32 v70, v67
	v_add_f32_e32 v67, 1.0, v71
	v_pk_mul_f32 v[64:65], v[64:65], v[66:67] op_sel_hi:[1,0]
	s_nop 0
	v_mul_f32_e32 v71, 0x3dd2d3e8, v64
	v_fma_f32 v71, -v64, v71, s0
	v_mul_f32_e32 v71, v64, v71
	v_exp_f32_e32 v72, v71
	v_mul_f32_e32 v71, 0x3dd2d3e8, v65
	v_fma_f32 v71, -v65, v71, s0
	v_mul_f32_e32 v71, v65, v71
	v_exp_f32_e32 v73, v71
	v_rcp_f32_e32 v71, v67
	v_add_f32_e32 v67, 1.0, v72
	v_rcp_f32_e32 v72, v67
	v_add_f32_e32 v67, 1.0, v73
	v_pk_mul_f32 v[58:59], v[58:59], v[66:67] op_sel_hi:[1,0]
	v_pk_mul_f32 v[62:63], v[62:63], v[70:71]
	v_mul_f32_e32 v73, 0x3dd2d3e8, v58
	v_fma_f32 v73, -v58, v73, s0
	v_mul_f32_e32 v73, v58, v73
	v_exp_f32_e32 v74, v73
	v_mul_f32_e32 v73, 0x3dd2d3e8, v59
	v_fma_f32 v73, -v59, v73, s0
	v_mul_f32_e32 v73, v59, v73
	v_exp_f32_e32 v75, v73
	v_rcp_f32_e32 v73, v67
	v_add_f32_e32 v67, 1.0, v74
	v_rcp_f32_e32 v74, v67
	v_add_f32_e32 v67, 1.0, v75
	v_pk_mul_f32 v[60:61], v[60:61], v[66:67] op_sel_hi:[1,0]
	v_pk_mul_f32 v[64:65], v[64:65], v[72:73]
	v_mul_f32_e32 v75, 0x3dd2d3e8, v60
	v_fma_f32 v75, -v60, v75, s0
	v_mul_f32_e32 v75, v60, v75
	v_exp_f32_e32 v76, v75
	v_mul_f32_e32 v75, 0x3dd2d3e8, v61
	v_fma_f32 v75, -v61, v75, s0
	v_mul_f32_e32 v75, v61, v75
	v_exp_f32_e32 v77, v75
	v_rcp_f32_e32 v75, v67
	v_add_f32_e32 v67, 1.0, v76
	v_rcp_f32_e32 v76, v67
	v_add_f32_e32 v67, 1.0, v77
	v_pk_mul_f32 v[54:55], v[54:55], v[66:67] op_sel_hi:[1,0]
	v_pk_mul_f32 v[70:71], v[58:59], v[74:75]
	v_cvt_pk_bf16_f32 v58, v62, v63
	v_mul_f32_e32 v62, 0x3dd2d3e8, v54
	v_mul_f32_e32 v63, 0x3dd2d3e8, v55
	v_rcp_f32_e32 v77, v67
	v_fma_f32 v62, -v54, v62, s0
	v_fma_f32 v63, -v55, v63, s0
	v_mul_f32_e32 v62, v54, v62
	v_mul_f32_e32 v63, v55, v63
	v_exp_f32_e32 v62, v62
	v_exp_f32_e32 v63, v63
	v_pk_mul_f32 v[72:73], v[60:61], v[76:77]
	v_cvt_pk_bf16_f32 v59, v64, v65
	v_cvt_pk_bf16_f32 v60, v70, v71
	v_cvt_pk_bf16_f32 v61, v72, v73
	v_pk_mul_f32 v[56:57], v[56:57], v[66:67] op_sel_hi:[1,0]
	v_pk_mul_f32 v[50:51], v[50:51], v[66:67] op_sel_hi:[1,0]
	v_pk_mul_f32 v[52:53], v[52:53], v[66:67] op_sel_hi:[1,0]
	global_store_dwordx4 v[68:69], v[58:61], off
	v_mul_f32_e32 v64, 0x3dd2d3e8, v52
	v_mul_f32_e32 v65, 0x3dd2d3e8, v53
	v_add_f32_e32 v58, 1.0, v62
	v_add_f32_e32 v59, 1.0, v63
	v_mul_f32_e32 v60, 0x3dd2d3e8, v56
	v_mul_f32_e32 v61, 0x3dd2d3e8, v57
	v_mul_f32_e32 v62, 0x3dd2d3e8, v50
	v_mul_f32_e32 v63, 0x3dd2d3e8, v51
	v_fma_f32 v60, -v56, v60, s0
	v_fma_f32 v61, -v57, v61, s0
	v_fma_f32 v62, -v50, v62, s0
	v_fma_f32 v63, -v51, v63, s0
	v_fma_f32 v64, -v52, v64, s0
	v_fma_f32 v65, -v53, v65, s0
	v_mul_f32_e32 v60, v56, v60
	v_mul_f32_e32 v61, v57, v61
	v_mul_f32_e32 v62, v50, v62
	v_mul_f32_e32 v63, v51, v63
	v_mul_f32_e32 v64, v52, v64
	v_mul_f32_e32 v65, v53, v65
	v_exp_f32_e32 v60, v60
	v_exp_f32_e32 v61, v61
	v_exp_f32_e32 v62, v62
	v_exp_f32_e32 v63, v63
	v_exp_f32_e32 v64, v64
	v_exp_f32_e32 v65, v65
	v_add_f32_e32 v60, 1.0, v60
	v_add_f32_e32 v61, 1.0, v61
	v_add_f32_e32 v62, 1.0, v62
	v_add_f32_e32 v63, 1.0, v63
	v_add_f32_e32 v64, 1.0, v64
	v_add_f32_e32 v65, 1.0, v65
	v_rcp_f32_e32 v58, v58
	v_rcp_f32_e32 v59, v59
	v_rcp_f32_e32 v60, v60
	v_rcp_f32_e32 v61, v61
	v_rcp_f32_e32 v62, v62
	v_rcp_f32_e32 v63, v63
	v_rcp_f32_e32 v64, v64
	v_rcp_f32_e32 v65, v65
	v_pk_mul_f32 v[54:55], v[54:55], v[58:59]
	v_pk_mul_f32 v[56:57], v[56:57], v[60:61]
	v_pk_mul_f32 v[58:59], v[50:51], v[62:63]
	v_pk_mul_f32 v[60:61], v[52:53], v[64:65]
	v_cvt_pk_bf16_f32 v50, v54, v55
	v_cvt_pk_bf16_f32 v51, v56, v57
	v_cvt_pk_bf16_f32 v52, v58, v59
	v_cvt_pk_bf16_f32 v53, v60, v61
	v_add_u32_e32 v66, 0x90, v0
	v_mov_b32_e32 v67, v1
	global_store_dwordx4 v[68:69], v[50:53], off offset:256
	s_nop 1
	v_lshlrev_b64 v[50:51], 6, v[66:67]
	v_lshl_add_u64 v[68:69], s[10:11], 0, v[50:51]
	s_nop 0
	s_nop 0
	v_mad_i64_i32 v[52:53], s[2:3], v66, s4, 0
	v_mov_b32_e32 v50, v217
	v_lshl_add_u64 v[52:53], v[52:53], 1, s[8:9]
	v_lshl_add_u64 v[52:53], v[52:53], 0, v[130:131]
	v_pk_mul_f32 v[46:47], v[46:47], v[50:51] op_sel_hi:[1,0]
	s_nop 0
	v_mul_f32_e32 v51, 0x3dd2d3e8, v46
	v_fma_f32 v51, -v46, v51, s0
	v_mul_f32_e32 v54, 0x3dd2d3e8, v47
	v_mul_f32_e32 v51, v46, v51
	v_fma_f32 v54, -v47, v54, s0
	v_exp_f32_e32 v51, v51
	v_mul_f32_e32 v54, v47, v54
	v_exp_f32_e32 v55, v54
	v_add_f32_e32 v51, 1.0, v51
	v_rcp_f32_e32 v54, v51
	v_add_f32_e32 v51, 1.0, v55
	v_pk_mul_f32 v[48:49], v[48:49], v[50:51] op_sel_hi:[1,0]
	s_nop 0
	v_mul_f32_e32 v55, 0x3dd2d3e8, v48
	v_fma_f32 v55, -v48, v55, s0
	v_mul_f32_e32 v55, v48, v55
	v_exp_f32_e32 v56, v55
	v_mul_f32_e32 v55, 0x3dd2d3e8, v49
	v_fma_f32 v55, -v49, v55, s0
	v_mul_f32_e32 v55, v49, v55
	v_exp_f32_e32 v57, v55
	v_rcp_f32_e32 v55, v51
	v_add_f32_e32 v51, 1.0, v56
	v_rcp_f32_e32 v56, v51
	v_add_f32_e32 v51, 1.0, v57
	v_pk_mul_f32 v[42:43], v[42:43], v[50:51] op_sel_hi:[1,0]
	v_pk_mul_f32 v[46:47], v[46:47], v[54:55]
	v_mul_f32_e32 v57, 0x3dd2d3e8, v42
	v_fma_f32 v57, -v42, v57, s0
	v_mul_f32_e32 v57, v42, v57
	v_exp_f32_e32 v58, v57
	v_mul_f32_e32 v57, 0x3dd2d3e8, v43
	v_fma_f32 v57, -v43, v57, s0
	v_mul_f32_e32 v57, v43, v57
	v_exp_f32_e32 v59, v57
	v_rcp_f32_e32 v57, v51
	v_add_f32_e32 v51, 1.0, v58
	v_rcp_f32_e32 v58, v51
	v_add_f32_e32 v51, 1.0, v59
	v_pk_mul_f32 v[44:45], v[44:45], v[50:51] op_sel_hi:[1,0]
	v_pk_mul_f32 v[48:49], v[48:49], v[56:57]
	v_mul_f32_e32 v59, 0x3dd2d3e8, v44
	v_fma_f32 v59, -v44, v59, s0
	v_mul_f32_e32 v59, v44, v59
	v_exp_f32_e32 v60, v59
	v_mul_f32_e32 v59, 0x3dd2d3e8, v45
	v_fma_f32 v59, -v45, v59, s0
	v_mul_f32_e32 v59, v45, v59
	v_exp_f32_e32 v61, v59
	v_rcp_f32_e32 v59, v51
	v_add_f32_e32 v51, 1.0, v60
	v_rcp_f32_e32 v60, v51
	v_add_f32_e32 v51, 1.0, v61
	v_pk_mul_f32 v[38:39], v[38:39], v[50:51] op_sel_hi:[1,0]
	v_pk_mul_f32 v[54:55], v[42:43], v[58:59]
	v_cvt_pk_bf16_f32 v42, v46, v47
	v_mul_f32_e32 v46, 0x3dd2d3e8, v38
	v_mul_f32_e32 v47, 0x3dd2d3e8, v39
	v_rcp_f32_e32 v61, v51
	v_fma_f32 v46, -v38, v46, s0
	v_fma_f32 v47, -v39, v47, s0
	v_mul_f32_e32 v46, v38, v46
	v_mul_f32_e32 v47, v39, v47
	v_exp_f32_e32 v46, v46
	v_exp_f32_e32 v47, v47
	v_pk_mul_f32 v[56:57], v[44:45], v[60:61]
	v_cvt_pk_bf16_f32 v43, v48, v49
	v_cvt_pk_bf16_f32 v44, v54, v55
	v_cvt_pk_bf16_f32 v45, v56, v57
	v_pk_mul_f32 v[40:41], v[40:41], v[50:51] op_sel_hi:[1,0]
	v_pk_mul_f32 v[34:35], v[34:35], v[50:51] op_sel_hi:[1,0]
	v_pk_mul_f32 v[36:37], v[36:37], v[50:51] op_sel_hi:[1,0]
	global_store_dwordx4 v[52:53], v[42:45], off
	v_mul_f32_e32 v48, 0x3dd2d3e8, v36
	v_mul_f32_e32 v49, 0x3dd2d3e8, v37
	v_add_f32_e32 v42, 1.0, v46
	v_add_f32_e32 v43, 1.0, v47
	v_mul_f32_e32 v44, 0x3dd2d3e8, v40
	v_mul_f32_e32 v45, 0x3dd2d3e8, v41
	v_mul_f32_e32 v46, 0x3dd2d3e8, v34
	v_mul_f32_e32 v47, 0x3dd2d3e8, v35
	v_fma_f32 v44, -v40, v44, s0
	v_fma_f32 v45, -v41, v45, s0
	v_fma_f32 v46, -v34, v46, s0
	v_fma_f32 v47, -v35, v47, s0
	v_fma_f32 v48, -v36, v48, s0
	v_fma_f32 v49, -v37, v49, s0
	v_mul_f32_e32 v44, v40, v44
	v_mul_f32_e32 v45, v41, v45
	v_mul_f32_e32 v46, v34, v46
	v_mul_f32_e32 v47, v35, v47
	v_mul_f32_e32 v48, v36, v48
	v_mul_f32_e32 v49, v37, v49
	v_exp_f32_e32 v44, v44
	v_exp_f32_e32 v45, v45
	v_exp_f32_e32 v46, v46
	v_exp_f32_e32 v47, v47
	v_exp_f32_e32 v48, v48
	v_exp_f32_e32 v49, v49
	v_add_f32_e32 v44, 1.0, v44
	v_add_f32_e32 v45, 1.0, v45
	v_add_f32_e32 v46, 1.0, v46
	v_add_f32_e32 v47, 1.0, v47
	v_add_f32_e32 v48, 1.0, v48
	v_add_f32_e32 v49, 1.0, v49
	v_rcp_f32_e32 v42, v42
	v_rcp_f32_e32 v43, v43
	v_rcp_f32_e32 v44, v44
	v_rcp_f32_e32 v45, v45
	v_rcp_f32_e32 v46, v46
	v_rcp_f32_e32 v47, v47
	v_rcp_f32_e32 v48, v48
	v_rcp_f32_e32 v49, v49
	v_pk_mul_f32 v[38:39], v[38:39], v[42:43]
	v_pk_mul_f32 v[40:41], v[40:41], v[44:45]
	v_pk_mul_f32 v[42:43], v[34:35], v[46:47]
	v_pk_mul_f32 v[44:45], v[36:37], v[48:49]
	v_cvt_pk_bf16_f32 v34, v38, v39
	v_cvt_pk_bf16_f32 v35, v40, v41
	v_cvt_pk_bf16_f32 v36, v42, v43
	v_cvt_pk_bf16_f32 v37, v44, v45
	v_add_u32_e32 v50, 0xa0, v0
	v_mov_b32_e32 v51, v1
	global_store_dwordx4 v[52:53], v[34:37], off offset:256
	v_add_u32_e32 v0, 0xb0, v0
	s_nop 0
	v_lshlrev_b64 v[34:35], 6, v[50:51]
	v_lshl_add_u64 v[52:53], s[10:11], 0, v[34:35]
	s_nop 0
	s_nop 0
	v_mad_i64_i32 v[36:37], s[2:3], v50, s4, 0
	v_mov_b32_e32 v34, v218
	v_lshl_add_u64 v[36:37], v[36:37], 1, s[8:9]
	v_lshl_add_u64 v[36:37], v[36:37], 0, v[130:131]
	v_pk_mul_f32 v[30:31], v[30:31], v[34:35] op_sel_hi:[1,0]
	s_nop 0
	v_mul_f32_e32 v35, 0x3dd2d3e8, v30
	v_fma_f32 v35, -v30, v35, s0
	v_mul_f32_e32 v38, 0x3dd2d3e8, v31
	v_mul_f32_e32 v35, v30, v35
	v_fma_f32 v38, -v31, v38, s0
	v_exp_f32_e32 v35, v35
	v_mul_f32_e32 v38, v31, v38
	v_exp_f32_e32 v39, v38
	v_add_f32_e32 v35, 1.0, v35
	v_rcp_f32_e32 v38, v35
	v_add_f32_e32 v35, 1.0, v39
	v_pk_mul_f32 v[32:33], v[32:33], v[34:35] op_sel_hi:[1,0]
	s_nop 0
	v_mul_f32_e32 v39, 0x3dd2d3e8, v32
	v_fma_f32 v39, -v32, v39, s0
	v_mul_f32_e32 v39, v32, v39
	v_exp_f32_e32 v40, v39
	v_mul_f32_e32 v39, 0x3dd2d3e8, v33
	v_fma_f32 v39, -v33, v39, s0
	v_mul_f32_e32 v39, v33, v39
	v_exp_f32_e32 v41, v39
	v_rcp_f32_e32 v39, v35
	v_add_f32_e32 v35, 1.0, v40
	v_rcp_f32_e32 v40, v35
	v_add_f32_e32 v35, 1.0, v41
	v_pk_mul_f32 v[26:27], v[26:27], v[34:35] op_sel_hi:[1,0]
	v_pk_mul_f32 v[30:31], v[30:31], v[38:39]
	v_mul_f32_e32 v41, 0x3dd2d3e8, v26
	v_fma_f32 v41, -v26, v41, s0
	v_mul_f32_e32 v41, v26, v41
	v_exp_f32_e32 v42, v41
	v_mul_f32_e32 v41, 0x3dd2d3e8, v27
	v_fma_f32 v41, -v27, v41, s0
	v_mul_f32_e32 v41, v27, v41
	v_exp_f32_e32 v43, v41
	v_rcp_f32_e32 v41, v35
	v_add_f32_e32 v35, 1.0, v42
	v_rcp_f32_e32 v42, v35
	v_add_f32_e32 v35, 1.0, v43
	v_pk_mul_f32 v[28:29], v[28:29], v[34:35] op_sel_hi:[1,0]
	v_pk_mul_f32 v[32:33], v[32:33], v[40:41]
	v_mul_f32_e32 v43, 0x3dd2d3e8, v28
	v_fma_f32 v43, -v28, v43, s0
	v_mul_f32_e32 v43, v28, v43
	v_exp_f32_e32 v44, v43
	v_mul_f32_e32 v43, 0x3dd2d3e8, v29
	v_fma_f32 v43, -v29, v43, s0
	v_mul_f32_e32 v43, v29, v43
	v_exp_f32_e32 v45, v43
	v_rcp_f32_e32 v43, v35
	v_add_f32_e32 v35, 1.0, v44
	v_rcp_f32_e32 v44, v35
	v_add_f32_e32 v35, 1.0, v45
	v_pk_mul_f32 v[22:23], v[22:23], v[34:35] op_sel_hi:[1,0]
	v_pk_mul_f32 v[38:39], v[26:27], v[42:43]
	v_cvt_pk_bf16_f32 v26, v30, v31
	v_mul_f32_e32 v30, 0x3dd2d3e8, v22
	v_mul_f32_e32 v31, 0x3dd2d3e8, v23
	v_rcp_f32_e32 v45, v35
	v_fma_f32 v30, -v22, v30, s0
	v_fma_f32 v31, -v23, v31, s0
	v_mul_f32_e32 v30, v22, v30
	v_mul_f32_e32 v31, v23, v31
	v_exp_f32_e32 v30, v30
	v_exp_f32_e32 v31, v31
	v_pk_mul_f32 v[40:41], v[28:29], v[44:45]
	v_cvt_pk_bf16_f32 v27, v32, v33
	v_cvt_pk_bf16_f32 v28, v38, v39
	v_cvt_pk_bf16_f32 v29, v40, v41
	v_pk_mul_f32 v[24:25], v[24:25], v[34:35] op_sel_hi:[1,0]
	v_pk_mul_f32 v[18:19], v[18:19], v[34:35] op_sel_hi:[1,0]
	v_pk_mul_f32 v[20:21], v[20:21], v[34:35] op_sel_hi:[1,0]
	global_store_dwordx4 v[36:37], v[26:29], off
	v_mul_f32_e32 v32, 0x3dd2d3e8, v20
	v_mul_f32_e32 v33, 0x3dd2d3e8, v21
	v_add_f32_e32 v26, 1.0, v30
	v_add_f32_e32 v27, 1.0, v31
	v_mul_f32_e32 v28, 0x3dd2d3e8, v24
	v_mul_f32_e32 v29, 0x3dd2d3e8, v25
	v_mul_f32_e32 v30, 0x3dd2d3e8, v18
	v_mul_f32_e32 v31, 0x3dd2d3e8, v19
	v_fma_f32 v28, -v24, v28, s0
	v_fma_f32 v29, -v25, v29, s0
	v_fma_f32 v30, -v18, v30, s0
	v_fma_f32 v31, -v19, v31, s0
	v_fma_f32 v32, -v20, v32, s0
	v_fma_f32 v33, -v21, v33, s0
	v_mul_f32_e32 v28, v24, v28
	v_mul_f32_e32 v29, v25, v29
	v_mul_f32_e32 v30, v18, v30
	v_mul_f32_e32 v31, v19, v31
	v_mul_f32_e32 v32, v20, v32
	v_mul_f32_e32 v33, v21, v33
	v_exp_f32_e32 v28, v28
	v_exp_f32_e32 v29, v29
	v_exp_f32_e32 v30, v30
	v_exp_f32_e32 v31, v31
	v_exp_f32_e32 v32, v32
	v_exp_f32_e32 v33, v33
	v_add_f32_e32 v28, 1.0, v28
	v_add_f32_e32 v29, 1.0, v29
	v_add_f32_e32 v30, 1.0, v30
	v_add_f32_e32 v31, 1.0, v31
	v_add_f32_e32 v32, 1.0, v32
	v_add_f32_e32 v33, 1.0, v33
	v_rcp_f32_e32 v26, v26
	v_rcp_f32_e32 v27, v27
	v_rcp_f32_e32 v28, v28
	v_rcp_f32_e32 v29, v29
	v_rcp_f32_e32 v30, v30
	v_rcp_f32_e32 v31, v31
	v_rcp_f32_e32 v32, v32
	v_rcp_f32_e32 v33, v33
	v_pk_mul_f32 v[22:23], v[22:23], v[26:27]
	v_pk_mul_f32 v[24:25], v[24:25], v[28:29]
	v_pk_mul_f32 v[26:27], v[18:19], v[30:31]
	v_pk_mul_f32 v[28:29], v[20:21], v[32:33]
	v_cvt_pk_bf16_f32 v18, v22, v23
	v_cvt_pk_bf16_f32 v19, v24, v25
	v_cvt_pk_bf16_f32 v20, v26, v27
	v_cvt_pk_bf16_f32 v21, v28, v29
	global_store_dwordx4 v[36:37], v[18:21], off offset:256
	s_nop 1
	v_lshlrev_b64 v[18:19], 6, v[0:1]
	v_lshl_add_u64 v[34:35], s[10:11], 0, v[18:19]
	s_nop 0
	s_nop 0
	s_nop 0
	v_mov_b32_e32 v18, v219
	v_mad_i64_i32 v[0:1], s[2:3], v0, s4, 0
	v_lshl_add_u64 v[0:1], v[0:1], 1, s[8:9]
	v_pk_mul_f32 v[14:15], v[14:15], v[18:19] op_sel_hi:[1,0]
	s_nop 0
	v_mul_f32_e32 v19, 0x3dd2d3e8, v14
	v_fma_f32 v19, -v14, v19, s0
	v_mul_f32_e32 v19, v14, v19
	v_mul_f32_e32 v20, 0x3dd2d3e8, v15
	v_exp_f32_e32 v19, v19
	v_fma_f32 v20, -v15, v20, s0
	v_mul_f32_e32 v20, v15, v20
	v_exp_f32_e32 v22, v20
	v_pk_mul_f32 v[16:17], v[16:17], v[18:19] op_sel_hi:[1,0]
	v_lshl_add_u64 v[20:21], v[0:1], 0, v[130:131]
	v_add_f32_e32 v0, 1.0, v19
	v_mul_f32_e32 v19, 0x3dd2d3e8, v16
	v_add_f32_e32 v1, 1.0, v22
	v_fma_f32 v19, -v16, v19, s0
	v_mul_f32_e32 v22, 0x3dd2d3e8, v17
	v_mul_f32_e32 v19, v16, v19
	v_fma_f32 v22, -v17, v22, s0
	v_exp_f32_e32 v19, v19
	v_mul_f32_e32 v22, v17, v22
	v_exp_f32_e32 v23, v22
	v_rcp_f32_e32 v0, v0
	v_add_f32_e32 v19, 1.0, v19
	v_rcp_f32_e32 v22, v19
	v_add_f32_e32 v19, 1.0, v23
	v_pk_mul_f32 v[10:11], v[10:11], v[18:19] op_sel_hi:[1,0]
	v_rcp_f32_e32 v1, v1
	v_mul_f32_e32 v23, 0x3dd2d3e8, v10
	v_fma_f32 v23, -v10, v23, s0
	v_mul_f32_e32 v23, v10, v23
	v_exp_f32_e32 v24, v23
	v_mul_f32_e32 v23, 0x3dd2d3e8, v11
	v_fma_f32 v23, -v11, v23, s0
	v_mul_f32_e32 v23, v11, v23
	v_exp_f32_e32 v25, v23
	v_rcp_f32_e32 v23, v19
	v_add_f32_e32 v19, 1.0, v24
	v_rcp_f32_e32 v24, v19
	v_add_f32_e32 v19, 1.0, v25
	v_pk_mul_f32 v[12:13], v[12:13], v[18:19] op_sel_hi:[1,0]
	v_pk_mul_f32 v[0:1], v[14:15], v[0:1]
	v_mul_f32_e32 v25, 0x3dd2d3e8, v12
	v_fma_f32 v25, -v12, v25, s0
	v_mul_f32_e32 v25, v12, v25
	v_exp_f32_e32 v26, v25
	v_mul_f32_e32 v25, 0x3dd2d3e8, v13
	v_fma_f32 v25, -v13, v25, s0
	v_mul_f32_e32 v25, v13, v25
	v_exp_f32_e32 v27, v25
	v_rcp_f32_e32 v25, v19
	v_add_f32_e32 v19, 1.0, v26
	v_rcp_f32_e32 v26, v19
	v_add_f32_e32 v19, 1.0, v27
	v_rcp_f32_e32 v27, v19
	v_pk_mul_f32 v[14:15], v[16:17], v[22:23]
	v_pk_mul_f32 v[16:17], v[10:11], v[24:25]
	v_cvt_pk_bf16_f32 v10, v0, v1
	v_pk_mul_f32 v[22:23], v[12:13], v[26:27]
	v_cvt_pk_bf16_f32 v11, v14, v15
	v_cvt_pk_bf16_f32 v12, v16, v17
	v_cvt_pk_bf16_f32 v13, v22, v23
	v_pk_mul_f32 v[0:1], v[6:7], v[18:19] op_sel_hi:[1,0]
	v_pk_mul_f32 v[8:9], v[8:9], v[18:19] op_sel_hi:[1,0]
	v_pk_mul_f32 v[2:3], v[2:3], v[18:19] op_sel_hi:[1,0]
	v_pk_mul_f32 v[4:5], v[4:5], v[18:19] op_sel_hi:[1,0]
	v_mul_f32_e32 v6, 0x3dd2d3e8, v0
	v_mul_f32_e32 v7, 0x3dd2d3e8, v1
	global_store_dwordx4 v[20:21], v[10:13], off
	v_mul_f32_e32 v14, 0x3dd2d3e8, v4
	v_mul_f32_e32 v15, 0x3dd2d3e8, v5
	v_mul_f32_e32 v10, 0x3dd2d3e8, v8
	v_mul_f32_e32 v11, 0x3dd2d3e8, v9
	v_mul_f32_e32 v12, 0x3dd2d3e8, v2
	v_mul_f32_e32 v13, 0x3dd2d3e8, v3
	v_fma_f32 v6, -v0, v6, s0
	v_fma_f32 v7, -v1, v7, s0
	v_fma_f32 v10, -v8, v10, s0
	v_fma_f32 v11, -v9, v11, s0
	v_fma_f32 v12, -v2, v12, s0
	v_fma_f32 v13, -v3, v13, s0
	v_fma_f32 v14, -v4, v14, s0
	v_fma_f32 v15, -v5, v15, s0
	v_mul_f32_e32 v6, v0, v6
	v_mul_f32_e32 v7, v1, v7
	v_mul_f32_e32 v10, v8, v10
	v_mul_f32_e32 v11, v9, v11
	v_mul_f32_e32 v12, v2, v12
	v_mul_f32_e32 v13, v3, v13
	v_mul_f32_e32 v14, v4, v14
	v_mul_f32_e32 v15, v5, v15
	v_exp_f32_e32 v6, v6
	v_exp_f32_e32 v7, v7
	v_exp_f32_e32 v10, v10
	v_exp_f32_e32 v11, v11
	v_exp_f32_e32 v12, v12
	v_exp_f32_e32 v13, v13
	v_exp_f32_e32 v14, v14
	v_exp_f32_e32 v15, v15
	v_add_f32_e32 v6, 1.0, v6
	v_add_f32_e32 v7, 1.0, v7
	v_add_f32_e32 v10, 1.0, v10
	v_add_f32_e32 v11, 1.0, v11
	v_add_f32_e32 v12, 1.0, v12
	v_add_f32_e32 v13, 1.0, v13
	v_add_f32_e32 v14, 1.0, v14
	v_add_f32_e32 v15, 1.0, v15
	v_rcp_f32_e32 v6, v6
	v_rcp_f32_e32 v7, v7
	v_rcp_f32_e32 v10, v10
	v_rcp_f32_e32 v11, v11
	v_rcp_f32_e32 v12, v12
	v_rcp_f32_e32 v13, v13
	v_rcp_f32_e32 v14, v14
	v_rcp_f32_e32 v15, v15
	v_pk_mul_f32 v[0:1], v[0:1], v[6:7]
	v_pk_mul_f32 v[6:7], v[8:9], v[10:11]
	v_pk_mul_f32 v[2:3], v[2:3], v[12:13]
	v_pk_mul_f32 v[4:5], v[4:5], v[14:15]
	v_cvt_pk_bf16_f32 v0, v0, v1
	v_cvt_pk_bf16_f32 v1, v6, v7
	v_cvt_pk_bf16_f32 v2, v2, v3
	v_cvt_pk_bf16_f32 v3, v4, v5
	global_store_dwordx4 v[20:21], v[0:3], off offset:256
	s_endpgm
	.p2align	8
